# speedup vs baseline: 1.0562x; 1.0077x over previous
_Z16node_post_kernelPKfS0_PKtS0_S2_S0_S0_S0_S0_S0_Pf:
	s_load_dwordx16 s[4:19], s[0:1], 0x0
	s_load_dwordx4 s[20:23], s[0:1], 0x40
	s_load_dwordx2 s[24:25], s[0:1], 0x50
	v_lshrrev_b32_e32 v5, 6, v0
	v_and_b32_e32 v1, 63, v0
	v_and_b32_e32 v2, 15, v0
	v_bfe_u32 v3, v0, 4, 2
	v_readfirstlane_b32 s26, v5
	v_lshlrev_b32_e32 v4, 4, v1
	v_lshlrev_b32_e32 v6, 5, v1
	v_add_u32_e32 v7, 0x1000, v6
	v_lshlrev_b32_e32 v8, 2, v1
	v_add_u32_e32 v9, 0x1000, v4
	v_add_u32_e32 v10, 0x2000, v4
	v_add_u32_e32 v11, 0x3000, v4
	v_lshlrev_b32_e32 v12, 7, v5
	v_lshl_or_b32 v12, v3, 4, v12
	v_and_b32_e32 v13, 1, v2
	v_lshl_or_b32 v13, v13, 10, v12
	v_mov_b32_e32 v14, 0xff7fffff
	v_cmp_gt_u32_e64 s[58:59], 2, v2
	s_lshl_b32 s27, s2, 1
	s_lshr_b32 s28, s2, 7
	s_and_b32 s29, s26, 1
	s_add_u32 s32, s27, s29
	s_lshl_b32 s32, s32, 13
	s_lshr_b32 s33, s26, 1
	s_lshl_b32 s33, s33, 3
	s_add_u32 s32, s32, s33
	s_lshl_b32 s60, s26, 14
	s_lshl_b32 s61, s28, 17
	s_add_u32 s61, s61, s60
	s_lshl_b32 s62, s28, 10
	s_lshl_b32 s63, s27, 10
	s_waitcnt lgkmcnt(0)
	s_add_u32 s30, s4, s32
	s_addc_u32 s31, s5, 0
	s_add_u32 s34, s6, s62
	s_addc_u32 s35, s7, 0
	s_add_u32 s36, s8, s61
	s_addc_u32 s37, s9, 0
	s_add_u32 s38, s12, s60
	s_addc_u32 s39, s13, 0
	s_add_u32 s40, s38, 0x20000
	s_addc_u32 s41, s39, 0
	s_add_u32 s42, s38, 0x40000
	s_addc_u32 s43, s39, 0
	s_add_u32 s44, s10, s63
	s_addc_u32 s45, s11, 0
	s_add_u32 s46, s24, s63
	s_addc_u32 s47, s25, 0
	global_load_dwordx2 v[56:57], v6, s[30:31]
	global_load_dwordx2 v[58:59], v6, s[30:31] offset:2048
	global_load_dwordx2 v[60:61], v7, s[30:31]
	global_load_dwordx2 v[62:63], v7, s[30:31] offset:2048
	global_load_dword v40, v8, s[34:35]
	global_load_dword v41, v8, s[34:35] offset:256
	global_load_dword v42, v8, s[34:35] offset:512
	global_load_dword v43, v8, s[34:35] offset:768
	global_load_dwordx4 v[64:67], v4, s[36:37]
	global_load_dwordx4 v[68:71], v4, s[36:37] offset:1024
	global_load_dwordx4 v[72:75], v4, s[36:37] offset:2048
	global_load_dwordx4 v[76:79], v4, s[36:37] offset:3072
	global_load_dwordx4 v[80:83], v9, s[36:37]
	global_load_dwordx4 v[84:87], v9, s[36:37] offset:1024
	global_load_dwordx4 v[88:91], v9, s[36:37] offset:2048
	global_load_dwordx4 v[92:95], v9, s[36:37] offset:3072
	global_load_dwordx4 v[96:99], v10, s[36:37]
	global_load_dwordx4 v[100:103], v10, s[36:37] offset:1024
	global_load_dwordx4 v[104:107], v10, s[36:37] offset:2048
	global_load_dwordx4 v[108:111], v10, s[36:37] offset:3072
	global_load_dwordx4 v[112:115], v11, s[36:37]
	global_load_dwordx4 v[116:119], v11, s[36:37] offset:1024
	global_load_dwordx4 v[120:123], v11, s[36:37] offset:2048
	global_load_dwordx4 v[124:127], v11, s[36:37] offset:3072
	global_load_dwordx4 v[16:19], v12, s[14:15]
	global_load_dwordx4 v[20:23], v12, s[14:15] offset:64
	global_load_dwordx4 v[24:27], v13, s[44:45]
	global_load_dwordx4 v[28:31], v13, s[44:45] offset:64
	global_load_dwordx4 v[32:35], v4, s[16:17]
	global_load_dwordx4 v[36:39], v4, s[18:19]
	global_load_dwordx4 v[128:131], v4, s[38:39]
	global_load_dwordx4 v[132:135], v4, s[38:39] offset:1024
	global_load_dwordx4 v[136:139], v4, s[38:39] offset:2048
	global_load_dwordx4 v[140:143], v4, s[38:39] offset:3072
	global_load_dwordx4 v[144:147], v9, s[38:39]
	global_load_dwordx4 v[148:151], v9, s[38:39] offset:1024
	global_load_dwordx4 v[152:155], v9, s[38:39] offset:2048
	global_load_dwordx4 v[156:159], v9, s[38:39] offset:3072
	global_load_dwordx4 v[160:163], v10, s[38:39]
	global_load_dwordx4 v[164:167], v10, s[38:39] offset:1024
	global_load_dwordx4 v[168:171], v10, s[38:39] offset:2048
	global_load_dwordx4 v[172:175], v10, s[38:39] offset:3072
	global_load_dwordx4 v[176:179], v11, s[38:39]
	global_load_dwordx4 v[180:183], v11, s[38:39] offset:1024
	global_load_dwordx4 v[184:187], v11, s[38:39] offset:2048
	global_load_dwordx4 v[188:191], v11, s[38:39] offset:3072
	global_load_dwordx4 v[192:195], v4, s[40:41]
	global_load_dwordx4 v[196:199], v4, s[40:41] offset:1024
	global_load_dwordx4 v[200:203], v4, s[40:41] offset:2048
	global_load_dwordx4 v[204:207], v4, s[40:41] offset:3072
	global_load_dwordx4 v[208:211], v9, s[40:41]
	global_load_dwordx4 v[212:215], v9, s[40:41] offset:1024
	global_load_dwordx4 v[216:219], v9, s[40:41] offset:2048
	global_load_dwordx4 v[220:223], v9, s[40:41] offset:3072
	global_load_dwordx4 v[224:227], v10, s[40:41]
	global_load_dwordx4 v[228:231], v10, s[40:41] offset:1024
	global_load_dwordx4 v[232:235], v10, s[40:41] offset:2048
	global_load_dwordx4 v[236:239], v10, s[40:41] offset:3072
	global_load_dwordx4 v[240:243], v11, s[40:41]
	global_load_dwordx4 v[244:247], v11, s[40:41] offset:1024
	global_load_dwordx4 v[248:251], v11, s[40:41] offset:2048
	global_load_dwordx4 v[252:255], v11, s[40:41] offset:3072
	v_lshlrev_b32_e32 v15, 1, v1
	s_lshl_b32 s48, s29, 12
	s_lshl_b32 s49, s33, 7
	s_add_u32 s48, s48, s49
	v_add_u32_e32 v15, s48, v15
	s_waitcnt vmcnt(54)
	v_cmp_neq_f32_e64 s[50:51], 0, v40
	v_cmp_neq_f32_e64 s[52:53], 0, v41
	v_cmp_neq_f32_e64 s[54:55], 0, v42
	v_cmp_neq_f32_e64 s[56:57], 0, v43
	v_cndmask_b32_e64 v56, v14, v56, s[50:51]
	v_cndmask_b32_e64 v57, v14, v57, s[50:51]
	v_cndmask_b32_e64 v58, v14, v58, s[52:53]
	v_cndmask_b32_e64 v59, v14, v59, s[52:53]
	v_cndmask_b32_e64 v60, v14, v60, s[54:55]
	v_cndmask_b32_e64 v61, v14, v61, s[54:55]
	v_cndmask_b32_e64 v62, v14, v62, s[56:57]
	v_cndmask_b32_e64 v63, v14, v63, s[56:57]
	v_max_f32_e32 v40, v56, v58
	v_max_f32_e32 v41, v57, v59
	v_max3_f32 v40, v40, v60, v62
	v_max3_f32 v41, v41, v61, v63
	s_nop 1
	v_max_f32_dpp v40, v40, v40 quad_perm:[1,0,3,2] row_mask:0xf bank_mask:0xf
	v_max_f32_dpp v41, v41, v41 quad_perm:[1,0,3,2] row_mask:0xf bank_mask:0xf
	s_nop 1
	v_max_f32_dpp v40, v40, v40 quad_perm:[2,3,0,1] row_mask:0xf bank_mask:0xf
	v_max_f32_dpp v41, v41, v41 quad_perm:[2,3,0,1] row_mask:0xf bank_mask:0xf
	s_nop 1
	v_max_f32_dpp v40, v40, v40 row_half_mirror row_mask:0xf bank_mask:0xf
	v_max_f32_dpp v41, v41, v41 row_half_mirror row_mask:0xf bank_mask:0xf
	s_nop 1
	v_max_f32_dpp v40, v40, v40 row_mirror row_mask:0xf bank_mask:0xf
	v_max_f32_dpp v41, v41, v41 row_mirror row_mask:0xf bank_mask:0xf
	s_nop 1
	v_mov_b32_e32 v42, v40
	v_mov_b32_e32 v43, v41
	s_nop 1
	v_permlane16_swap_b32_e32 v40, v42
	v_permlane16_swap_b32_e32 v41, v43
	v_max_f32_e32 v40, v40, v42
	v_max_f32_e32 v41, v41, v43
	v_mov_b32_e32 v42, v40
	v_mov_b32_e32 v43, v41
	s_nop 1
	v_permlane32_swap_b32_e32 v40, v42
	v_permlane32_swap_b32_e32 v41, v43
	v_max_f32_e32 v40, v40, v42
	v_max_f32_e32 v41, v41, v43
	v_sub_f32_e32 v56, v56, v40
	v_sub_f32_e32 v57, v57, v41
	v_sub_f32_e32 v58, v58, v40
	v_sub_f32_e32 v59, v59, v41
	v_sub_f32_e32 v60, v60, v40
	v_sub_f32_e32 v61, v61, v41
	v_sub_f32_e32 v62, v62, v40
	v_sub_f32_e32 v63, v63, v41
	v_mul_f32_e32 v56, 0x3fb8aa3b, v56
	v_mul_f32_e32 v57, 0x3fb8aa3b, v57
	v_mul_f32_e32 v58, 0x3fb8aa3b, v58
	v_mul_f32_e32 v59, 0x3fb8aa3b, v59
	v_mul_f32_e32 v60, 0x3fb8aa3b, v60
	v_mul_f32_e32 v61, 0x3fb8aa3b, v61
	v_mul_f32_e32 v62, 0x3fb8aa3b, v62
	v_mul_f32_e32 v63, 0x3fb8aa3b, v63
	v_exp_f32_e32 v56, v56
	v_exp_f32_e32 v57, v57
	v_exp_f32_e32 v58, v58
	v_exp_f32_e32 v59, v59
	v_exp_f32_e32 v60, v60
	v_exp_f32_e32 v61, v61
	v_exp_f32_e32 v62, v62
	v_exp_f32_e32 v63, v63
	s_nop 0
	v_add_f32_e32 v44, v56, v58
	v_add_f32_e32 v45, v57, v59
	v_add_f32_e32 v44, v44, v60
	v_add_f32_e32 v45, v45, v61
	v_add_f32_e32 v44, v44, v62
	v_add_f32_e32 v45, v45, v63
	s_nop 1
	v_add_f32_dpp v44, v44, v44 quad_perm:[1,0,3,2] row_mask:0xf bank_mask:0xf
	v_add_f32_dpp v45, v45, v45 quad_perm:[1,0,3,2] row_mask:0xf bank_mask:0xf
	s_nop 1
	v_add_f32_dpp v44, v44, v44 quad_perm:[2,3,0,1] row_mask:0xf bank_mask:0xf
	v_add_f32_dpp v45, v45, v45 quad_perm:[2,3,0,1] row_mask:0xf bank_mask:0xf
	s_nop 1
	v_add_f32_dpp v44, v44, v44 row_half_mirror row_mask:0xf bank_mask:0xf
	v_add_f32_dpp v45, v45, v45 row_half_mirror row_mask:0xf bank_mask:0xf
	s_nop 1
	v_add_f32_dpp v44, v44, v44 row_mirror row_mask:0xf bank_mask:0xf
	v_add_f32_dpp v45, v45, v45 row_mirror row_mask:0xf bank_mask:0xf
	s_nop 1
	v_mov_b32_e32 v42, v44
	v_mov_b32_e32 v43, v45
	s_nop 1
	v_permlane16_swap_b32_e32 v44, v42
	v_permlane16_swap_b32_e32 v45, v43
	v_add_f32_e32 v44, v44, v42
	v_add_f32_e32 v45, v45, v43
	v_mov_b32_e32 v42, v44
	v_mov_b32_e32 v43, v45
	s_nop 1
	v_permlane32_swap_b32_e32 v44, v42
	v_permlane32_swap_b32_e32 v45, v43
	v_add_f32_e32 v44, v44, v42
	v_add_f32_e32 v45, v45, v43
	v_rcp_f32_e32 v46, v44
	v_rcp_f32_e32 v47, v45
	s_nop 0
	v_fma_f32 v42, -v44, v46, 1.0
	v_fma_f32 v43, -v45, v47, 1.0
	v_fma_f32 v46, v42, v46, v46
	v_fma_f32 v47, v43, v47, v47
	v_mul_f32_e32 v56, v56, v46
	v_mul_f32_e32 v57, v57, v47
	v_mul_f32_e32 v58, v58, v46
	v_mul_f32_e32 v59, v59, v47
	v_mul_f32_e32 v60, v60, v46
	v_mul_f32_e32 v61, v61, v47
	v_mul_f32_e32 v62, v62, v46
	v_mul_f32_e32 v63, v63, v47
	v_cvt_pk_bf16_f32 v48, v56, v57
	v_cvt_pk_bf16_f32 v49, v58, v59
	v_cvt_pk_bf16_f32 v50, v60, v61
	v_cvt_pk_bf16_f32 v51, v62, v63
	ds_write_b16 v15, v48 offset:0
	ds_write_b16_d16_hi v15, v48 offset:512
	ds_write_b16 v15, v49 offset:128
	ds_write_b16_d16_hi v15, v49 offset:640
	ds_write_b16 v15, v50 offset:256
	ds_write_b16_d16_hi v15, v50 offset:768
	ds_write_b16 v15, v51 offset:384
	ds_write_b16_d16_hi v15, v51 offset:896
	v_lshlrev_b32_e32 v6, 12, v2
	v_lshl_or_b32 v6, v5, 9, v6
	v_lshl_or_b32 v6, v3, 4, v6
	v_lshlrev_b32_e32 v7, 9, v2
	v_lshl_or_b32 v7, v3, 4, v7
	v_lshlrev_b32_e32 v8, 9, v2
	v_lshl_or_b32 v8, v5, 6, v8
	v_lshl_or_b32 v8, v3, 3, v8
	v_mov_b32_e32 v40, 0
	v_mov_b32_e32 v41, 0
	v_mov_b32_e32 v42, 0
	v_mov_b32_e32 v43, 0
	v_mov_b32_e32 v44, 0
	v_mov_b32_e32 v45, 0
	v_mov_b32_e32 v46, 0
	v_mov_b32_e32 v47, 0
	v_mov_b32_e32 v48, 0
	v_mov_b32_e32 v49, 0
	v_mov_b32_e32 v50, 0
	v_mov_b32_e32 v51, 0
	v_mov_b32_e32 v52, 0
	v_mov_b32_e32 v53, 0
	v_mov_b32_e32 v54, 0
	v_mov_b32_e32 v55, 0
	s_waitcnt lgkmcnt(0)
	s_barrier
	s_waitcnt vmcnt(38)
	s_mov_b64 exec, s[58:59]
	ds_read_b128 v[40:43], v6 offset:0
	ds_read_b128 v[44:47], v6 offset:64
	ds_read_b128 v[48:51], v6 offset:128
	ds_read_b128 v[52:55], v6 offset:192
	s_mov_b64 exec, -1
	s_waitcnt lgkmcnt(0)
	v_mfma_f32_16x16x32_bf16 v[56:59], v[64:67], v[40:43], 0
	v_mfma_f32_16x16x32_bf16 v[60:63], v[96:99], v[40:43], 0
	v_mfma_f32_16x16x32_bf16 v[56:59], v[68:71], v[44:47], v[56:59]
	v_mfma_f32_16x16x32_bf16 v[60:63], v[100:103], v[44:47], v[60:63]
	v_mfma_f32_16x16x32_bf16 v[56:59], v[72:75], v[48:51], v[56:59]
	v_mfma_f32_16x16x32_bf16 v[60:63], v[104:107], v[48:51], v[60:63]
	v_mfma_f32_16x16x32_bf16 v[56:59], v[76:79], v[52:55], v[56:59]
	v_mfma_f32_16x16x32_bf16 v[60:63], v[108:111], v[52:55], v[60:63]
	s_mov_b64 exec, s[58:59]
	ds_read_b128 v[40:43], v6 offset:256
	ds_read_b128 v[44:47], v6 offset:320
	ds_read_b128 v[48:51], v6 offset:384
	ds_read_b128 v[52:55], v6 offset:448
	s_mov_b64 exec, -1
	s_waitcnt lgkmcnt(0)
	v_mfma_f32_16x16x32_bf16 v[56:59], v[80:83], v[40:43], v[56:59]
	v_mfma_f32_16x16x32_bf16 v[60:63], v[112:115], v[40:43], v[60:63]
	v_mfma_f32_16x16x32_bf16 v[56:59], v[84:87], v[44:47], v[56:59]
	v_mfma_f32_16x16x32_bf16 v[60:63], v[116:119], v[44:47], v[60:63]
	v_mfma_f32_16x16x32_bf16 v[56:59], v[88:91], v[48:51], v[56:59]
	v_mfma_f32_16x16x32_bf16 v[60:63], v[120:123], v[48:51], v[60:63]
	v_mfma_f32_16x16x32_bf16 v[56:59], v[92:95], v[52:55], v[56:59]
	v_mfma_f32_16x16x32_bf16 v[60:63], v[124:127], v[52:55], v[60:63]
	s_nop 9
	v_cvt_pk_bf16_f32 v48, v56, v57
	v_cvt_pk_bf16_f32 v49, v58, v59
	v_cvt_pk_bf16_f32 v50, v60, v61
	v_cvt_pk_bf16_f32 v51, v62, v63
	s_mov_b64 exec, s[58:59]
	ds_write_b64 v8, v[48:49] offset:8192
	ds_write_b64 v8, v[50:51] offset:8224
	s_mov_b64 exec, -1
	global_load_dwordx4 v[64:67], v4, s[42:43]
	global_load_dwordx4 v[68:71], v4, s[42:43] offset:1024
	global_load_dwordx4 v[72:75], v4, s[42:43] offset:2048
	global_load_dwordx4 v[76:79], v4, s[42:43] offset:3072
	global_load_dwordx4 v[80:83], v9, s[42:43]
	global_load_dwordx4 v[84:87], v9, s[42:43] offset:1024
	global_load_dwordx4 v[88:91], v9, s[42:43] offset:2048
	global_load_dwordx4 v[92:95], v9, s[42:43] offset:3072
	global_load_dwordx4 v[96:99], v10, s[42:43]
	global_load_dwordx4 v[100:103], v10, s[42:43] offset:1024
	global_load_dwordx4 v[104:107], v10, s[42:43] offset:2048
	global_load_dwordx4 v[108:111], v10, s[42:43] offset:3072
	global_load_dwordx4 v[112:115], v11, s[42:43]
	global_load_dwordx4 v[116:119], v11, s[42:43] offset:1024
	global_load_dwordx4 v[120:123], v11, s[42:43] offset:2048
	global_load_dwordx4 v[124:127], v11, s[42:43] offset:3072
	v_lshlrev_b32_e32 v15, 10, v2
	v_add_u32_e32 v15, v15, v12
	v_mov_b32_e32 v48, 0
	v_mov_b32_e32 v49, 0
	v_mov_b32_e32 v50, 0
	v_mov_b32_e32 v51, 0
	s_waitcnt lgkmcnt(0)
	s_barrier
	s_waitcnt vmcnt(32)
	s_mov_b64 exec, s[58:59]
	ds_read_b128 v[40:43], v7 offset:8192
	ds_read_b128 v[44:47], v7 offset:8256
	ds_read_b128 v[48:51], v7 offset:8320
	ds_read_b128 v[52:55], v7 offset:8384
	s_mov_b64 exec, -1
	s_waitcnt lgkmcnt(0)
	v_mfma_f32_16x16x32_bf16 v[56:59], v[128:131], v[40:43], 0
	v_mfma_f32_16x16x32_bf16 v[60:63], v[160:163], v[40:43], 0
	v_mfma_f32_16x16x32_bf16 v[56:59], v[132:135], v[44:47], v[56:59]
	v_mfma_f32_16x16x32_bf16 v[60:63], v[164:167], v[44:47], v[60:63]
	v_mfma_f32_16x16x32_bf16 v[56:59], v[136:139], v[48:51], v[56:59]
	v_mfma_f32_16x16x32_bf16 v[60:63], v[168:171], v[48:51], v[60:63]
	v_mfma_f32_16x16x32_bf16 v[56:59], v[140:143], v[52:55], v[56:59]
	v_mfma_f32_16x16x32_bf16 v[60:63], v[172:175], v[52:55], v[60:63]
	s_mov_b64 exec, s[58:59]
	ds_read_b128 v[40:43], v7 offset:8448
	ds_read_b128 v[44:47], v7 offset:8512
	ds_read_b128 v[48:51], v7 offset:8576
	ds_read_b128 v[52:55], v7 offset:8640
	s_mov_b64 exec, -1
	s_waitcnt lgkmcnt(0)
	v_mfma_f32_16x16x32_bf16 v[56:59], v[144:147], v[40:43], v[56:59]
	v_mfma_f32_16x16x32_bf16 v[60:63], v[176:179], v[40:43], v[60:63]
	v_mfma_f32_16x16x32_bf16 v[56:59], v[148:151], v[44:47], v[56:59]
	v_mfma_f32_16x16x32_bf16 v[60:63], v[180:183], v[44:47], v[60:63]
	v_mfma_f32_16x16x32_bf16 v[56:59], v[152:155], v[48:51], v[56:59]
	v_mfma_f32_16x16x32_bf16 v[60:63], v[184:187], v[48:51], v[60:63]
	v_mfma_f32_16x16x32_bf16 v[56:59], v[156:159], v[52:55], v[56:59]
	v_mfma_f32_16x16x32_bf16 v[60:63], v[188:191], v[52:55], v[60:63]
	s_nop 9
	v_add_f32_e32 v56, v56, v16
	v_add_f32_e32 v57, v57, v17
	v_add_f32_e32 v58, v58, v18
	v_add_f32_e32 v59, v59, v19
	v_add_f32_e32 v60, v60, v20
	v_add_f32_e32 v61, v61, v21
	v_add_f32_e32 v62, v62, v22
	v_add_f32_e32 v63, v63, v23
	v_add_f32_e32 v24, v56, v24
	v_add_f32_e32 v25, v57, v25
	v_add_f32_e32 v26, v58, v26
	v_add_f32_e32 v27, v59, v27
	v_add_f32_e32 v28, v60, v28
	v_add_f32_e32 v29, v61, v29
	v_add_f32_e32 v30, v62, v30
	v_add_f32_e32 v31, v63, v31
	s_mov_b64 exec, s[58:59]
	ds_write_b128 v15, v[24:27] offset:10240
	ds_write_b128 v15, v[28:31] offset:10304
	s_mov_b64 exec, -1
	global_load_dwordx4 v[16:19], v12, s[20:21]
	global_load_dwordx4 v[20:23], v12, s[20:21] offset:64
	s_waitcnt lgkmcnt(0)
	s_barrier
	s_cmp_gt_u32 s26, 1
	s_cbranch_scc1 .Lnp_ln_done
	s_lshl_b32 s48, s26, 10
	v_add_u32_e32 v40, s48, v4
	ds_read_b128 v[44:47], v40 offset:10240
	s_waitcnt lgkmcnt(0)
	v_add_f32_e32 v41, v44, v45
	v_add_f32_e32 v41, v41, v46
	v_add_f32_e32 v41, v41, v47
	s_nop 1
	v_add_f32_dpp v41, v41, v41 quad_perm:[1,0,3,2] row_mask:0xf bank_mask:0xf
	s_nop 1
	v_add_f32_dpp v41, v41, v41 quad_perm:[2,3,0,1] row_mask:0xf bank_mask:0xf
	s_nop 1
	v_add_f32_dpp v41, v41, v41 row_half_mirror row_mask:0xf bank_mask:0xf
	s_nop 1
	v_add_f32_dpp v41, v41, v41 row_mirror row_mask:0xf bank_mask:0xf
	s_nop 1
	v_mov_b32_e32 v42, v41
	s_nop 1
	v_permlane16_swap_b32_e32 v41, v42
	v_add_f32_e32 v41, v41, v42
	v_mov_b32_e32 v42, v41
	s_nop 1
	v_permlane32_swap_b32_e32 v41, v42
	v_add_f32_e32 v41, v41, v42
	v_mul_f32_e32 v41, 0x3b800000, v41
	v_sub_f32_e32 v44, v44, v41
	v_sub_f32_e32 v45, v45, v41
	v_sub_f32_e32 v46, v46, v41
	v_sub_f32_e32 v47, v47, v41
	v_mul_f32_e32 v43, v44, v44
	v_fmac_f32_e32 v43, v45, v45
	v_fmac_f32_e32 v43, v46, v46
	v_fmac_f32_e32 v43, v47, v47
	s_nop 1
	v_add_f32_dpp v43, v43, v43 quad_perm:[1,0,3,2] row_mask:0xf bank_mask:0xf
	s_nop 1
	v_add_f32_dpp v43, v43, v43 quad_perm:[2,3,0,1] row_mask:0xf bank_mask:0xf
	s_nop 1
	v_add_f32_dpp v43, v43, v43 row_half_mirror row_mask:0xf bank_mask:0xf
	s_nop 1
	v_add_f32_dpp v43, v43, v43 row_mirror row_mask:0xf bank_mask:0xf
	s_nop 1
	v_mov_b32_e32 v42, v43
	s_nop 1
	v_permlane16_swap_b32_e32 v43, v42
	v_add_f32_e32 v43, v43, v42
	v_mov_b32_e32 v42, v43
	s_nop 1
	v_permlane32_swap_b32_e32 v43, v42
	v_add_f32_e32 v43, v43, v42
	v_mov_b32_e32 v42, 0x3727c5ac
	v_fmac_f32_e32 v42, 0x3b800000, v43
	v_rsq_f32_e32 v42, v42
	s_nop 0
	v_mul_f32_e32 v44, v44, v42
	v_mul_f32_e32 v45, v45, v42
	v_mul_f32_e32 v46, v46, v42
	v_mul_f32_e32 v47, v47, v42
	v_fma_f32 v44, v44, v32, v36
	v_fma_f32 v45, v45, v33, v37
	v_fma_f32 v46, v46, v34, v38
	v_fma_f32 v47, v47, v35, v39
	v_cvt_pk_bf16_f32 v48, v44, v45
	v_cvt_pk_bf16_f32 v49, v46, v47
	s_lshl_b32 s48, s26, 9
	v_lshlrev_b32_e32 v40, 3, v1
	v_add_u32_e32 v40, s48, v40
	ds_write_b64 v40, v[48:49] offset:8192
	v_mov_b32_e32 v40, 0
	v_mov_b32_e32 v41, 0
	v_mov_b32_e32 v42, 0
	v_mov_b32_e32 v43, 0
	v_mov_b32_e32 v44, 0
	v_mov_b32_e32 v45, 0
	v_mov_b32_e32 v46, 0
	v_mov_b32_e32 v47, 0
	v_mov_b32_e32 v48, 0
	v_mov_b32_e32 v49, 0
	v_mov_b32_e32 v50, 0
	v_mov_b32_e32 v51, 0
.Lnp_ln_done:
	s_waitcnt lgkmcnt(0)
	s_barrier
	global_load_dwordx4 v[32:35], v12, s[22:23]
	global_load_dwordx4 v[36:39], v12, s[22:23] offset:64
	s_waitcnt vmcnt(20)
	s_mov_b64 exec, s[58:59]
	ds_read_b128 v[40:43], v7 offset:8192
	ds_read_b128 v[44:47], v7 offset:8256
	ds_read_b128 v[48:51], v7 offset:8320
	ds_read_b128 v[52:55], v7 offset:8384
	s_mov_b64 exec, -1
	s_waitcnt lgkmcnt(0)
	v_mfma_f32_16x16x32_bf16 v[56:59], v[192:195], v[40:43], 0
	v_mfma_f32_16x16x32_bf16 v[60:63], v[224:227], v[40:43], 0
	v_mfma_f32_16x16x32_bf16 v[56:59], v[196:199], v[44:47], v[56:59]
	v_mfma_f32_16x16x32_bf16 v[60:63], v[228:231], v[44:47], v[60:63]
	v_mfma_f32_16x16x32_bf16 v[56:59], v[200:203], v[48:51], v[56:59]
	v_mfma_f32_16x16x32_bf16 v[60:63], v[232:235], v[48:51], v[60:63]
	v_mfma_f32_16x16x32_bf16 v[56:59], v[204:207], v[52:55], v[56:59]
	v_mfma_f32_16x16x32_bf16 v[60:63], v[236:239], v[52:55], v[60:63]
	s_mov_b64 exec, s[58:59]
	ds_read_b128 v[40:43], v7 offset:8448
	ds_read_b128 v[44:47], v7 offset:8512
	ds_read_b128 v[48:51], v7 offset:8576
	ds_read_b128 v[52:55], v7 offset:8640
	s_mov_b64 exec, -1
	s_waitcnt lgkmcnt(0)
	v_mfma_f32_16x16x32_bf16 v[56:59], v[208:211], v[40:43], v[56:59]
	v_mfma_f32_16x16x32_bf16 v[60:63], v[240:243], v[40:43], v[60:63]
	v_mfma_f32_16x16x32_bf16 v[56:59], v[212:215], v[44:47], v[56:59]
	v_mfma_f32_16x16x32_bf16 v[60:63], v[244:247], v[44:47], v[60:63]
	v_mfma_f32_16x16x32_bf16 v[56:59], v[216:219], v[48:51], v[56:59]
	v_mfma_f32_16x16x32_bf16 v[60:63], v[248:251], v[48:51], v[60:63]
	v_mfma_f32_16x16x32_bf16 v[56:59], v[220:223], v[52:55], v[56:59]
	v_mfma_f32_16x16x32_bf16 v[60:63], v[252:255], v[52:55], v[60:63]
	s_nop 9
	s_waitcnt vmcnt(2)
	v_add_f32_e32 v56, v56, v16
	v_add_f32_e32 v57, v57, v17
	v_add_f32_e32 v58, v58, v18
	v_add_f32_e32 v59, v59, v19
	v_add_f32_e32 v60, v60, v20
	v_add_f32_e32 v61, v61, v21
	v_add_f32_e32 v62, v62, v22
	v_add_f32_e32 v63, v63, v23
	v_mul_f32_e32 v40, 0x3c23d70a, v56
	v_mul_f32_e32 v41, 0x3c23d70a, v57
	v_mul_f32_e32 v42, 0x3c23d70a, v58
	v_mul_f32_e32 v43, 0x3c23d70a, v59
	v_mul_f32_e32 v44, 0x3c23d70a, v60
	v_mul_f32_e32 v45, 0x3c23d70a, v61
	v_mul_f32_e32 v46, 0x3c23d70a, v62
	v_mul_f32_e32 v47, 0x3c23d70a, v63
	v_max_f32_e32 v56, v56, v40
	v_max_f32_e32 v57, v57, v41
	v_max_f32_e32 v58, v58, v42
	v_max_f32_e32 v59, v59, v43
	v_max_f32_e32 v60, v60, v44
	v_max_f32_e32 v61, v61, v45
	v_max_f32_e32 v62, v62, v46
	v_max_f32_e32 v63, v63, v47
	v_cvt_pk_bf16_f32 v48, v56, v57
	v_cvt_pk_bf16_f32 v49, v58, v59
	v_cvt_pk_bf16_f32 v50, v60, v61
	v_cvt_pk_bf16_f32 v51, v62, v63
	s_mov_b64 exec, s[58:59]
	ds_write_b64 v8, v[48:49] offset:9216
	ds_write_b64 v8, v[50:51] offset:9248
	s_mov_b64 exec, -1
	v_mov_b32_e32 v40, 0
	v_mov_b32_e32 v41, 0
	v_mov_b32_e32 v42, 0
	v_mov_b32_e32 v43, 0
	v_mov_b32_e32 v44, 0
	v_mov_b32_e32 v45, 0
	v_mov_b32_e32 v46, 0
	v_mov_b32_e32 v47, 0
	v_mov_b32_e32 v48, 0
	v_mov_b32_e32 v49, 0
	v_mov_b32_e32 v50, 0
	v_mov_b32_e32 v51, 0
	s_waitcnt lgkmcnt(0)
	s_barrier
	s_mov_b64 exec, s[58:59]
	ds_read_b128 v[40:43], v7 offset:9216
	ds_read_b128 v[44:47], v7 offset:9280
	ds_read_b128 v[48:51], v7 offset:9344
	ds_read_b128 v[52:55], v7 offset:9408
	s_mov_b64 exec, -1
	s_waitcnt lgkmcnt(0)
	v_mfma_f32_16x16x32_bf16 v[56:59], v[64:67], v[40:43], 0
	v_mfma_f32_16x16x32_bf16 v[60:63], v[96:99], v[40:43], 0
	v_mfma_f32_16x16x32_bf16 v[56:59], v[68:71], v[44:47], v[56:59]
	v_mfma_f32_16x16x32_bf16 v[60:63], v[100:103], v[44:47], v[60:63]
	v_mfma_f32_16x16x32_bf16 v[56:59], v[72:75], v[48:51], v[56:59]
	v_mfma_f32_16x16x32_bf16 v[60:63], v[104:107], v[48:51], v[60:63]
	v_mfma_f32_16x16x32_bf16 v[56:59], v[76:79], v[52:55], v[56:59]
	v_mfma_f32_16x16x32_bf16 v[60:63], v[108:111], v[52:55], v[60:63]
	s_mov_b64 exec, s[58:59]
	ds_read_b128 v[40:43], v7 offset:9472
	ds_read_b128 v[44:47], v7 offset:9536
	ds_read_b128 v[48:51], v7 offset:9600
	ds_read_b128 v[52:55], v7 offset:9664
	s_mov_b64 exec, -1
	s_waitcnt lgkmcnt(0)
	v_mfma_f32_16x16x32_bf16 v[56:59], v[80:83], v[40:43], v[56:59]
	v_mfma_f32_16x16x32_bf16 v[60:63], v[112:115], v[40:43], v[60:63]
	v_mfma_f32_16x16x32_bf16 v[56:59], v[84:87], v[44:47], v[56:59]
	v_mfma_f32_16x16x32_bf16 v[60:63], v[116:119], v[44:47], v[60:63]
	v_mfma_f32_16x16x32_bf16 v[56:59], v[88:91], v[48:51], v[56:59]
	v_mfma_f32_16x16x32_bf16 v[60:63], v[120:123], v[48:51], v[60:63]
	v_mfma_f32_16x16x32_bf16 v[56:59], v[92:95], v[52:55], v[56:59]
	v_mfma_f32_16x16x32_bf16 v[60:63], v[124:127], v[52:55], v[60:63]
	s_nop 9
	s_waitcnt vmcnt(0)
	v_add_f32_e32 v56, v56, v32
	v_add_f32_e32 v57, v57, v33
	v_add_f32_e32 v58, v58, v34
	v_add_f32_e32 v59, v59, v35
	v_add_f32_e32 v60, v60, v36
	v_add_f32_e32 v61, v61, v37
	v_add_f32_e32 v62, v62, v38
	v_add_f32_e32 v63, v63, v39
	v_mul_f32_e32 v40, 0x3c23d70a, v56
	v_mul_f32_e32 v41, 0x3c23d70a, v57
	v_mul_f32_e32 v42, 0x3c23d70a, v58
	v_mul_f32_e32 v43, 0x3c23d70a, v59
	v_mul_f32_e32 v44, 0x3c23d70a, v60
	v_mul_f32_e32 v45, 0x3c23d70a, v61
	v_mul_f32_e32 v46, 0x3c23d70a, v62
	v_mul_f32_e32 v47, 0x3c23d70a, v63
	v_max_f32_e32 v56, v56, v40
	v_max_f32_e32 v57, v57, v41
	v_max_f32_e32 v58, v58, v42
	v_max_f32_e32 v59, v59, v43
	v_max_f32_e32 v60, v60, v44
	v_max_f32_e32 v61, v61, v45
	v_max_f32_e32 v62, v62, v46
	v_max_f32_e32 v63, v63, v47
	v_add_f32_e32 v56, v56, v24
	v_add_f32_e32 v57, v57, v25
	v_add_f32_e32 v58, v58, v26
	v_add_f32_e32 v59, v59, v27
	v_add_f32_e32 v60, v60, v28
	v_add_f32_e32 v61, v61, v29
	v_add_f32_e32 v62, v62, v30
	v_add_f32_e32 v63, v63, v31
	s_mov_b64 exec, s[58:59]
	global_store_dwordx4 v13, v[56:59], s[46:47]
	global_store_dwordx4 v13, v[60:63], s[46:47] offset:64
	s_endpgm

	.amdhsa_kernel _Z16node_post_kernelPKfS0_PKtS0_S2_S0_S0_S0_S0_S0_Pf
		.amdhsa_group_segment_fixed_size 12288
		.amdhsa_private_segment_fixed_size 0
		.amdhsa_kernarg_size 88
		.amdhsa_user_sgpr_count 2
		.amdhsa_user_sgpr_dispatch_ptr 0
		.amdhsa_user_sgpr_queue_ptr 0
		.amdhsa_user_sgpr_kernarg_segment_ptr 1
		.amdhsa_user_sgpr_dispatch_id 0
		.amdhsa_user_sgpr_kernarg_preload_length 0
		.amdhsa_user_sgpr_kernarg_preload_offset 0
		.amdhsa_user_sgpr_private_segment_size 0
		.amdhsa_uses_dynamic_stack 0
		.amdhsa_enable_private_segment 0
		.amdhsa_system_sgpr_workgroup_id_x 1
		.amdhsa_system_sgpr_workgroup_id_y 0
		.amdhsa_system_sgpr_workgroup_id_z 0
		.amdhsa_system_sgpr_workgroup_info 0
		.amdhsa_system_vgpr_workitem_id 0
		.amdhsa_next_free_vgpr 256
		.amdhsa_next_free_sgpr 64
		.amdhsa_accum_offset 256
		.amdhsa_reserve_vcc 1
		.amdhsa_float_round_mode_32 0
		.amdhsa_float_round_mode_16_64 0
		.amdhsa_float_denorm_mode_32 3
		.amdhsa_float_denorm_mode_16_64 3
		.amdhsa_dx10_clamp 1
		.amdhsa_ieee_mode 1
		.amdhsa_fp16_overflow 0
		.amdhsa_tg_split 0
		.amdhsa_exception_fp_ieee_invalid_op 0
		.amdhsa_exception_fp_denorm_src 0
		.amdhsa_exception_fp_ieee_div_zero 0
		.amdhsa_exception_fp_ieee_overflow 0
		.amdhsa_exception_fp_ieee_underflow 0
		.amdhsa_exception_fp_ieee_inexact 0
		.amdhsa_exception_int_div_zero 0
	.end_amdhsa_kernel

amdhsa.kernels:
  - .agpr_count:     0
    .args:
      - .actual_access:  read_only
        .address_space:  global
        .offset:         0
        .size:           8
        .value_kind:     global_buffer
      - .actual_access:  read_only
        .address_space:  global
        .offset:         8
        .size:           8
        .value_kind:     global_buffer
      - .actual_access:  read_only
        .address_space:  global
        .offset:         16
        .size:           8
        .value_kind:     global_buffer
      - .actual_access:  read_only
        .address_space:  global
        .offset:         24
        .size:           8
        .value_kind:     global_buffer
      - .actual_access:  read_only
        .address_space:  global
        .offset:         32
        .size:           8
        .value_kind:     global_buffer
      - .actual_access:  read_only
        .address_space:  global
        .offset:         40
        .size:           8
        .value_kind:     global_buffer
      - .actual_access:  read_only
        .address_space:  global
        .offset:         48
        .size:           8
        .value_kind:     global_buffer
      - .actual_access:  read_only
        .address_space:  global
        .offset:         56
        .size:           8
        .value_kind:     global_buffer
      - .actual_access:  read_only
        .address_space:  global
        .offset:         64
        .size:           8
        .value_kind:     global_buffer
      - .actual_access:  read_only
        .address_space:  global
        .offset:         72
        .size:           8
        .value_kind:     global_buffer
      - .actual_access:  read_only
        .address_space:  global
        .offset:         80
        .size:           8
        .value_kind:     global_buffer
      - .actual_access:  write_only
        .address_space:  global
        .offset:         88
        .size:           8
        .value_kind:     global_buffer
      - .actual_access:  write_only
        .address_space:  global
        .offset:         96
        .size:           8
        .value_kind:     global_buffer
      - .actual_access:  read_only
        .address_space:  global
        .offset:         104
        .size:           8
        .value_kind:     global_buffer
      - .actual_access:  read_only
        .address_space:  global
        .offset:         112
        .size:           8
        .value_kind:     global_buffer
      - .actual_access:  read_only
        .address_space:  global
        .offset:         120
        .size:           8
        .value_kind:     global_buffer
      - .actual_access:  read_only
        .address_space:  global
        .offset:         128
        .size:           8
        .value_kind:     global_buffer
      - .actual_access:  read_only
        .address_space:  global
        .offset:         136
        .size:           8
        .value_kind:     global_buffer
      - .actual_access:  read_only
        .address_space:  global
        .offset:         144
        .size:           8
        .value_kind:     global_buffer
      - .actual_access:  write_only
        .address_space:  global
        .offset:         152
        .size:           8
        .value_kind:     global_buffer
      - .actual_access:  write_only
        .address_space:  global
        .offset:         160
        .size:           8
        .value_kind:     global_buffer
      - .actual_access:  write_only
        .address_space:  global
        .offset:         168
        .size:           8
        .value_kind:     global_buffer
      - .actual_access:  read_only
        .address_space:  global
        .offset:         176
        .size:           8
        .value_kind:     global_buffer
      - .actual_access:  read_only
        .address_space:  global
        .offset:         184
        .size:           8
        .value_kind:     global_buffer
      - .actual_access:  read_only
        .address_space:  global
        .offset:         192
        .size:           8
        .value_kind:     global_buffer
      - .actual_access:  write_only
        .address_space:  global
        .offset:         200
        .size:           8
        .value_kind:     global_buffer
    .group_segment_fixed_size: 40960
    .kernarg_segment_align: 8
    .kernarg_segment_size: 208
    .language:       OpenCL C
    .language_version:
      - 2
      - 0
    .max_flat_workgroup_size: 256
    .name:           _Z10pre_kernelPKfS0_S0_S0_S0_S0_S0_S0_S0_S0_S0_PtPfS0_S0_S0_S0_S0_S0_S2_S2_S2_S0_S0_S0_S1_
    .private_segment_fixed_size: 0
    .sgpr_count:     106
    .sgpr_spill_count: 0
    .symbol:         _Z10pre_kernelPKfS0_S0_S0_S0_S0_S0_S0_S0_S0_S0_PtPfS0_S0_S0_S0_S0_S0_S2_S2_S2_S0_S0_S0_S1_.kd
    .uniform_work_group_size: 1
    .uses_dynamic_stack: false
    .vgpr_count:     128
    .vgpr_spill_count: 0
    .wavefront_size: 64
  - .agpr_count:     0
    .args:
      - .actual_access:  read_only
        .address_space:  global
        .offset:         0
        .size:           8
        .value_kind:     global_buffer
      - .address_space:  global
        .offset:         8
        .size:           8
        .value_kind:     global_buffer
      - .address_space:  global
        .offset:         16
        .size:           8
        .value_kind:     global_buffer
      - .address_space:  global
        .offset:         24
        .size:           8
        .value_kind:     global_buffer
      - .address_space:  global
        .offset:         32
        .size:           8
        .value_kind:     global_buffer
      - .actual_access:  write_only
        .address_space:  global
        .offset:         40
        .size:           8
        .value_kind:     global_buffer
      - .actual_access:  write_only
        .address_space:  global
        .offset:         48
        .size:           8
        .value_kind:     global_buffer
    .group_segment_fixed_size: 79872
    .kernarg_segment_align: 8
    .kernarg_segment_size: 56
    .language:       OpenCL C
    .language_version:
      - 2
      - 0
    .max_flat_workgroup_size: 256
    .name:           _Z11edge_kernelPKfPK15HIP_vector_typeIjLj4EES0_S0_S4_PfS5_
    .private_segment_fixed_size: 0
    .sgpr_count:     26
    .sgpr_spill_count: 0
    .symbol:         _Z11edge_kernelPKfPK15HIP_vector_typeIjLj4EES0_S0_S4_PfS5_.kd
    .uniform_work_group_size: 1
    .uses_dynamic_stack: false
    .vgpr_count:     256
    .vgpr_spill_count: 0
    .wavefront_size: 64
  - .agpr_count:     0
    .args:
      - .actual_access:  read_only
        .address_space:  global
        .offset:         0
        .size:           8
        .value_kind:     global_buffer
      - .actual_access:  read_only
        .address_space:  global
        .offset:         8
        .size:           8
        .value_kind:     global_buffer
      - .actual_access:  read_only
        .address_space:  global
        .offset:         16
        .size:           8
        .value_kind:     global_buffer
      - .actual_access:  read_only
        .address_space:  global
        .offset:         24
        .size:           8
        .value_kind:     global_buffer
      - .actual_access:  read_only
        .address_space:  global
        .offset:         32
        .size:           8
        .value_kind:     global_buffer
      - .actual_access:  read_only
        .address_space:  global
        .offset:         40
        .size:           8
        .value_kind:     global_buffer
      - .actual_access:  read_only
        .address_space:  global
        .offset:         48
        .size:           8
        .value_kind:     global_buffer
      - .actual_access:  read_only
        .address_space:  global
        .offset:         56
        .size:           8
        .value_kind:     global_buffer
      - .actual_access:  read_only
        .address_space:  global
        .offset:         64
        .size:           8
        .value_kind:     global_buffer
      - .actual_access:  read_only
        .address_space:  global
        .offset:         72
        .size:           8
        .value_kind:     global_buffer
      - .actual_access:  write_only
        .address_space:  global
        .offset:         80
        .size:           8
        .value_kind:     global_buffer
    .group_segment_fixed_size: 12288
    .kernarg_segment_align: 8
    .kernarg_segment_size: 88
    .language:       OpenCL C
    .language_version:
      - 2
      - 0
    .max_flat_workgroup_size: 512
    .name:           _Z16node_post_kernelPKfS0_PKtS0_S2_S0_S0_S0_S0_S0_Pf
    .private_segment_fixed_size: 0
    .sgpr_count:     70
    .sgpr_spill_count: 0
    .symbol:         _Z16node_post_kernelPKfS0_PKtS0_S2_S0_S0_S0_S0_S0_Pf.kd
    .uniform_work_group_size: 1
    .uses_dynamic_stack: false
    .vgpr_count:     256
    .vgpr_spill_count: 0
    .wavefront_size: 64
